# attention/scan: first MFMA of each accumulation chain takes inline 0 as C (zero-init moves removed); attention unit-start wait counted
# baseline (speedup 1.0000x reference)
.LBB0_647:
	s_add_i32 s18, s8, 0x80
	s_cmp_lt_u32 s18, s16
	s_cselect_b64 s[6:7], -1, 0
	s_cmp_ge_u32 s18, s16
	s_cselect_b64 s[4:5], -1, 0
	s_and_b64 vcc, exec, s[4:5]
	s_movk_i32 s54, 0x1000
	s_cbranch_vccnz .LBB0_649
	s_add_i32 s9, s8, 0xfffffe80
	s_cmpk_gt_u32 s8, 0x17f
	s_cselect_b64 s[0:1], -1, 0
	s_and_b64 s[0:1], s[0:1], exec
	s_cselect_b32 s0, s9, s18
	s_cselect_b32 s9, 4, 32
	s_abs_i32 s1, s9
	v_cvt_f32_u32_e32 v5, s1
	s_sub_i32 s15, 0, s1
	s_abs_i32 s14, s0
	s_ashr_i32 s13, s0, 31
	v_rcp_iflag_f32_e32 v5, v5
	s_nop 0
	v_mul_f32_e32 v5, 0x4f7ffffe, v5
	v_cvt_u32_f32_e32 v5, v5
	s_nop 0
	v_readfirstlane_b32 s22, v5
	s_mul_i32 s15, s15, s22
	s_mul_hi_u32 s15, s22, s15
	s_add_i32 s22, s22, s15
	s_mul_hi_u32 s15, s14, s22
	s_mul_i32 s22, s15, s1
	s_sub_i32 s22, s14, s22
	s_add_i32 s23, s15, 1
	s_sub_i32 s24, s22, s1
	s_cmp_ge_u32 s22, s1
	s_cselect_b32 s15, s23, s15
	s_cselect_b32 s22, s24, s22
	s_add_i32 s23, s15, 1
	s_cmp_ge_u32 s22, s1
	s_cselect_b32 s1, s23, s15
	s_xor_b32 s1, s1, s13
	s_sub_i32 s15, s1, s13
	s_mul_i32 s1, s15, s9
	s_sub_i32 s23, s0, s1
	s_lshl_b32 s24, s23, 6
	s_sub_i32 s0, 0x840, s24
	s_min_u32 s0, s0, 0x100
	s_lshr_b32 s22, s0, 6
	s_cmpk_gt_u32 s8, 0x17f
	s_cselect_b64 s[0:1], -1, 0
	s_and_b64 s[0:1], s[0:1], exec
	s_cselect_b32 s26, -1, s22
	s_lshl_b32 s0, s9, 1
	v_cvt_f32_u32_e32 v5, s0
	s_sub_i32 s1, 0, s0
	v_rcp_iflag_f32_e32 v5, v5
	s_nop 0
	v_mul_f32_e32 v5, 0x4f7ffffe, v5
	v_cvt_u32_f32_e32 v6, v5
	v_mov_b32_e32 v5, v131
	v_readfirstlane_b32 s9, v6
	s_mul_i32 s1, s1, s9
	s_mul_hi_u32 s1, s9, s1
	s_add_i32 s9, s9, s1
	s_mul_hi_u32 s1, s14, s9
	s_mul_i32 s9, s1, s0
	s_sub_i32 s9, s14, s9
	s_add_i32 s22, s1, 1
	s_sub_i32 s14, s9, s0
	s_cmp_ge_u32 s9, s0
	s_cselect_b32 s1, s22, s1
	s_cselect_b32 s9, s14, s9
	s_add_i32 s14, s1, 1
	s_cmp_ge_u32 s9, s0
	s_cselect_b32 s0, s14, s1
	s_xor_b32 s0, s0, s13
	s_sub_i32 s0, s0, s13
	s_lshl_b32 s1, s0, 8
	s_lshl_b32 s13, s0, 11
	s_add_i32 s22, s1, 0x4000
	s_cmpk_gt_u32 s8, 0x17f
	s_cselect_b64 s[0:1], -1, 0
	s_and_b64 s[8:9], s[0:1], exec
	s_cselect_b32 s8, s22, s13
	s_lshr_b32 s9, s15, 31
	s_add_i32 s9, s15, s9
	s_add_i32 s8, s8, s24
	s_and_b32 s9, s9, -2
	v_or_b32_e32 v6, s8, v160
	s_sub_i32 s14, s15, s9
	v_ashrrev_i32_e32 v7, 31, v6
	v_readlane_b32 s8, v252, 20
	v_lshlrev_b64 v[6:7], 10, v[6:7]
	v_lshl_add_u32 v8, s14, 8, v161
	v_readlane_b32 s9, v252, 21
	v_ashrrev_i32_e32 v9, 31, v8
	s_add_i32 s13, s13, s24
	v_lshl_add_u64 v[6:7], s[8:9], 0, v[6:7]
	v_lshl_add_u64 v[6:7], v[8:9], 1, v[6:7]
	v_lshl_add_u64 v[4:5], v[6:7], 0, v[4:5]
	global_load_dwordx4 v[70:73], v[4:5], off
	global_load_dwordx4 v[74:77], v[4:5], off offset:32
	global_load_dwordx4 v[82:85], v[4:5], off offset:64
	global_load_dwordx4 v[86:89], v[4:5], off offset:96
	s_cmp_gt_i32 s23, 1
	s_cselect_b64 s[8:9], -1, 0
	s_or_b64 s[0:1], s[0:1], s[8:9]
	s_sub_i32 s8, 0x80, s24
	s_lshr_b32 s8, s8, 6
	s_and_b64 s[0:1], s[0:1], exec
	s_cselect_b32 s24, 0, s8
	s_sub_i32 s0, s26, s24
	s_lshl_b32 s8, s14, 6
	s_add_i32 s25, s13, 0xffffff80
	s_add_i32 s23, s0, 1
	s_ashr_i32 s9, s8, 31
	s_cmp_lt_i32 s20, -4
	v_mov_b32_e32 v42, 1.0
	s_cbranch_scc1 .LBB0_629
	s_waitcnt vmcnt(4)
	s_branch .LBB0_650
.LBB0_649:
	s_mov_b64 s[8:9], 0
	s_mov_b32 s23, 0
	s_mov_b32 s24, 0
	s_mov_b32 s22, 0
	s_mov_b32 s25, 0
	s_cmp_lt_i32 s20, -4
	v_mov_b32_e32 v42, 1.0
	s_cbranch_scc1 .LBB0_629
	s_waitcnt vmcnt(0)
.LBB0_650:
	s_add_i32 s27, s12, s10
	s_lshl_b32 s10, s11, 6
	v_mul_f32_e32 v179, 0x3fb8aa3b, v3
	s_add_i32 s26, s20, 5
	s_addk_i32 s27, 0xff80
	s_ashr_i32 s11, s10, 31
	s_mov_b32 s28, 0
	s_sub_i32 s29, 0, s23
	v_mov_b32_e32 v165, 1.0
	v_mov_b32_e32 v19, v18
	v_mov_b32_e32 v20, v18
	v_mov_b32_e32 v21, v18
	v_mov_b32_e32 v22, v18
	v_mov_b32_e32 v23, v18
	v_mov_b32_e32 v24, v18
	v_mov_b32_e32 v25, v18
	v_mov_b32_e32 v26, v18
	v_mov_b32_e32 v27, v18
	v_mov_b32_e32 v28, v18
	v_mov_b32_e32 v29, v18
	v_mov_b32_e32 v30, v18
	v_mov_b32_e32 v31, v18
	v_mov_b32_e32 v32, v18
	v_mov_b32_e32 v33, v18
	v_mov_b32_e32 v3, v2
	v_mov_b32_e32 v4, v2
	v_mov_b32_e32 v5, v2
	v_mov_b32_e32 v6, v2
	v_mov_b32_e32 v7, v2
	v_mov_b32_e32 v8, v2
	v_mov_b32_e32 v9, v2
	v_mov_b32_e32 v10, v2
	v_mov_b32_e32 v11, v2
	v_mov_b32_e32 v12, v2
	v_mov_b32_e32 v13, v2
	v_mov_b32_e32 v14, v2
	v_mov_b32_e32 v15, v2
	v_mov_b32_e32 v16, v2
	v_mov_b32_e32 v17, v2

.LBB0_663:
	v_add3_u32 v46, s30, v175, v170
	v_add3_u32 v50, s30, v176, v170
	ds_read_b128 v[34:37], v46
	ds_read_b128 v[38:41], v46 offset:32
	ds_read_b128 v[42:45], v46 offset:64
	ds_read_b128 v[46:49], v46 offset:96
	ds_read_b128 v[180:183], v50
	ds_read_b128 v[184:187], v50 offset:32
	ds_read_b128 v[188:191], v50 offset:64
	ds_read_b128 v[198:201], v50 offset:96
	v_add3_u32 v50, s30, v177, v162
	v_add3_u32 v51, s30, v178, v162
	v_add_u32_e32 v50, 0x2000, v50
	v_add_u32_e32 v51, 0x2000, v51
	ds_read2_b64 v[152:155], v50 offset0:128 offset1:130
	ds_read2_b64 v[144:147], v50 offset0:132 offset1:134
	ds_read2_b64 v[148:151], v51 offset0:128 offset1:130
	ds_read2_b64 v[140:143], v51 offset0:132 offset1:134
	ds_read2_b64 v[136:139], v50 offset0:136 offset1:138
	ds_read2_b64 v[132:135], v51 offset0:136 offset1:138
	ds_read2_b64 v[126:129], v50 offset0:140 offset1:142
	ds_read2_b64 v[122:125], v51 offset0:140 offset1:142
	s_waitcnt lgkmcnt(14)
	v_mfma_f32_32x32x16_bf16 v[50:65], v[34:37], v[98:101], 0
	v_mfma_f32_32x32x16_bf16 v[50:65], v[38:41], v[102:105], v[50:65]
	s_waitcnt lgkmcnt(13)
	v_mfma_f32_32x32x16_bf16 v[50:65], v[42:45], v[106:109], v[50:65]
	s_waitcnt lgkmcnt(12)
	v_mfma_f32_32x32x16_bf16 v[50:65], v[46:49], v[110:113], v[50:65]
	s_waitcnt lgkmcnt(11)
	v_mfma_f32_32x32x16_bf16 v[34:49], v[180:183], v[98:101], 0
	s_waitcnt lgkmcnt(10)
	v_mfma_f32_32x32x16_bf16 v[34:49], v[184:187], v[102:105], v[34:49]
	s_waitcnt lgkmcnt(9)
	v_mfma_f32_32x32x16_bf16 v[34:49], v[188:191], v[106:109], v[34:49]
	s_waitcnt lgkmcnt(8)
	v_mfma_f32_32x32x16_bf16 v[34:49], v[198:201], v[110:113], v[34:49]
	s_cmp_gt_i32 s28, s20
	s_cbranch_scc1 .LBB0_670
	s_add_i32 s14, s28, s19
	s_cmp_lt_i32 s14, 4
	s_cbranch_scc1 .LBB0_666
	s_cmp_eq_u32 s14, 4
	s_cselect_b64 s[0:1], -1, 0
	s_cbranch_execz .LBB0_667
	s_branch .LBB0_668

.LBB0_769:
	s_bitcmp1_b32 s68, 0
	s_cselect_b32 s8, 0x12000, 0
	v_add_u32_e32 v190, s8, v136
	ds_read_b128 v[98:101], v190
	ds_read_b128 v[138:141], v190 offset:1024
	ds_read_b128 v[102:105], v190 offset:16384
	ds_read_b128 v[142:145], v190 offset:17408
	ds_read_b128 v[146:149], v190 offset:8192
	ds_read_b128 v[150:153], v190 offset:9216
	ds_read_b128 v[154:157], v190 offset:24576
	ds_read_b128 v[158:161], v190 offset:25600
	v_add_u32_e32 v191, s49, v190
	ds_read_b128 v[162:165], v190 offset:2048
	ds_read_b128 v[166:169], v190 offset:3072
	ds_read_b128 v[170:173], v190 offset:18432
	ds_read_b128 v[174:177], v190 offset:19456
	ds_read_b128 v[178:181], v190 offset:10240
	ds_read_b128 v[182:185], v190 offset:11264
	ds_read_b128 v[186:189], v190 offset:26624
	ds_read_b128 v[198:201], v190 offset:27648
	v_cvt_pk_bf16_f32 v202, v2, v3
	v_cvt_pk_bf16_f32 v203, v4, v5
	v_cvt_pk_bf16_f32 v204, v6, v7
	v_cvt_pk_bf16_f32 v205, v8, v9
	s_waitcnt lgkmcnt(8)
	s_nop 0
	v_mfma_f32_32x32x16_bf16 v[114:129], v[98:101], v[202:205], 0
	v_mfma_f32_32x32x16_bf16 v[82:97], v[102:105], v[202:205], 0
	v_mfma_f32_32x32x16_bf16 v[98:113], v[146:149], v[202:205], 0
	v_cvt_pk_bf16_f32 v146, v10, v11
	v_cvt_pk_bf16_f32 v147, v12, v13
	v_cvt_pk_bf16_f32 v148, v14, v15
	v_cvt_pk_bf16_f32 v149, v16, v17
	v_mfma_f32_32x32x16_bf16 v[66:81], v[154:157], v[202:205], 0
	s_nop 0
	v_mfma_f32_32x32x16_bf16 v[82:97], v[142:145], v[146:149], v[82:97]
	v_mfma_f32_32x32x16_bf16 v[66:81], v[158:161], v[146:149], v[66:81]
	v_mfma_f32_32x32x16_bf16 v[114:129], v[138:141], v[146:149], v[114:129]
	v_mfma_f32_32x32x16_bf16 v[98:113], v[150:153], v[146:149], v[98:113]
	ds_read_b128 v[138:141], v190 offset:4096
	ds_read_b128 v[142:145], v190 offset:5120
	ds_read_b128 v[146:149], v190 offset:20480
	ds_read_b128 v[150:153], v190 offset:21504
	ds_read_b128 v[154:157], v190 offset:12288
	ds_read_b128 v[158:161], v190 offset:13312
	ds_read_b128 v[202:205], v190 offset:28672
	ds_read_b128 v[206:209], v190 offset:29696
	v_cvt_pk_bf16_f32 v210, v18, v19
	v_cvt_pk_bf16_f32 v211, v20, v21
	v_cvt_pk_bf16_f32 v212, v22, v23
	v_cvt_pk_bf16_f32 v213, v24, v25
	s_waitcnt lgkmcnt(8)
	s_nop 0
	v_mfma_f32_32x32x16_bf16 v[82:97], v[170:173], v[210:213], v[82:97]
	v_mfma_f32_32x32x16_bf16 v[66:81], v[186:189], v[210:213], v[66:81]
	v_mfma_f32_32x32x16_bf16 v[114:129], v[162:165], v[210:213], v[114:129]
	v_cvt_pk_bf16_f32 v162, v26, v27
	v_cvt_pk_bf16_f32 v163, v28, v29
	v_cvt_pk_bf16_f32 v164, v30, v31
	v_cvt_pk_bf16_f32 v165, v32, v33
	v_mfma_f32_32x32x16_bf16 v[98:113], v[178:181], v[210:213], v[98:113]
	s_nop 0
	v_mfma_f32_32x32x16_bf16 v[82:97], v[174:177], v[162:165], v[82:97]
	v_mfma_f32_32x32x16_bf16 v[66:81], v[198:201], v[162:165], v[66:81]
	v_mfma_f32_32x32x16_bf16 v[114:129], v[166:169], v[162:165], v[114:129]
	v_mfma_f32_32x32x16_bf16 v[98:113], v[182:185], v[162:165], v[98:113]
	ds_read_b128 v[162:165], v190 offset:6144
	ds_read_b128 v[166:169], v190 offset:7168
	ds_read_b128 v[170:173], v190 offset:22528
	ds_read_b128 v[174:177], v190 offset:23552
	ds_read_b128 v[178:181], v190 offset:14336
	ds_read_b128 v[182:185], v190 offset:15360
	ds_read_b128 v[186:189], v190 offset:30720
	ds_read_b128 v[198:201], v190 offset:31744
	v_cvt_pk_bf16_f32 v210, v34, v35
	v_cvt_pk_bf16_f32 v211, v36, v37
	v_cvt_pk_bf16_f32 v212, v38, v39
	v_cvt_pk_bf16_f32 v213, v40, v41
	s_waitcnt lgkmcnt(8)
	s_nop 0
	v_mfma_f32_32x32x16_bf16 v[82:97], v[146:149], v[210:213], v[82:97]
	v_mfma_f32_32x32x16_bf16 v[66:81], v[202:205], v[210:213], v[66:81]
	v_mfma_f32_32x32x16_bf16 v[114:129], v[138:141], v[210:213], v[114:129]
	v_cvt_pk_bf16_f32 v138, v42, v43
	v_cvt_pk_bf16_f32 v139, v44, v45
	v_cvt_pk_bf16_f32 v140, v46, v47
	v_cvt_pk_bf16_f32 v141, v48, v49
	v_mfma_f32_32x32x16_bf16 v[98:113], v[154:157], v[210:213], v[98:113]
	s_nop 0
	v_mfma_f32_32x32x16_bf16 v[82:97], v[150:153], v[138:141], v[82:97]
	v_mfma_f32_32x32x16_bf16 v[66:81], v[206:209], v[138:141], v[66:81]
	v_mfma_f32_32x32x16_bf16 v[114:129], v[142:145], v[138:141], v[114:129]
	v_mfma_f32_32x32x16_bf16 v[98:113], v[158:161], v[138:141], v[98:113]
	s_barrier
	ds_read_b128 v[138:141], v191 offset:57344
	ds_read_b128 v[142:145], v191 offset:58368
	ds_read_b128 v[146:149], v191 offset:59392
	ds_read_b128 v[150:153], v191 offset:60416
	ds_read_b128 v[154:157], v191 offset:61440
	ds_read_b128 v[158:161], v191 offset:62464
	ds_read_b128 v[202:205], v191 offset:63488
	ds_read_b128 v[206:209], v191 offset:64512
	v_cvt_pk_bf16_f32 v210, v50, v51
	v_cvt_pk_bf16_f32 v211, v52, v53
	v_cvt_pk_bf16_f32 v212, v54, v55
	v_cvt_pk_bf16_f32 v213, v56, v57
	s_waitcnt lgkmcnt(8)
	s_nop 0
	v_mfma_f32_32x32x16_bf16 v[82:97], v[170:173], v[210:213], v[82:97]
	v_mfma_f32_32x32x16_bf16 v[66:81], v[186:189], v[210:213], v[66:81]
	v_mfma_f32_32x32x16_bf16 v[114:129], v[162:165], v[210:213], v[114:129]
	v_cvt_pk_bf16_f32 v162, v58, v59
	v_cvt_pk_bf16_f32 v163, v60, v61
	v_cvt_pk_bf16_f32 v164, v62, v63
	v_cvt_pk_bf16_f32 v165, v64, v65
	v_mfma_f32_32x32x16_bf16 v[98:113], v[178:181], v[210:213], v[98:113]
	s_nop 0
	v_mfma_f32_32x32x16_bf16 v[82:97], v[174:177], v[162:165], v[82:97]
	v_mfma_f32_32x32x16_bf16 v[66:81], v[198:201], v[162:165], v[66:81]
	v_mfma_f32_32x32x16_bf16 v[114:129], v[166:169], v[162:165], v[114:129]
	v_mfma_f32_32x32x16_bf16 v[98:113], v[182:185], v[162:165], v[98:113]
	ds_read_b128 v[162:165], v190 offset:32768
	ds_read_b128 v[166:169], v190 offset:33792
	ds_read_b128 v[170:173], v190 offset:34816
	ds_read_b128 v[174:177], v190 offset:35840
	ds_read_b128 v[178:181], v190 offset:36864
	ds_read_b128 v[182:185], v190 offset:37888
	ds_read_b128 v[186:189], v190 offset:38912
	ds_read_b128 v[198:201], v190 offset:39936
	s_waitcnt lgkmcnt(8)
	s_nop 1
	v_pk_add_f32 v[114:115], v[138:139], v[114:115] neg_lo:[0,1] neg_hi:[0,1]
	v_pk_add_f32 v[116:117], v[140:141], v[116:117] neg_lo:[0,1] neg_hi:[0,1]
	v_pk_add_f32 v[118:119], v[142:143], v[118:119] neg_lo:[0,1] neg_hi:[0,1]
	v_pk_add_f32 v[122:123], v[146:147], v[122:123] neg_lo:[0,1] neg_hi:[0,1]
	v_pk_add_f32 v[120:121], v[144:145], v[120:121] neg_lo:[0,1] neg_hi:[0,1]
	v_pk_add_f32 v[124:125], v[148:149], v[124:125] neg_lo:[0,1] neg_hi:[0,1]
	v_pk_add_f32 v[126:127], v[150:151], v[126:127] neg_lo:[0,1] neg_hi:[0,1]
	v_cvt_pk_bf16_f32 v114, v114, v115
	v_cvt_pk_bf16_f32 v115, v116, v117
	v_cvt_pk_bf16_f32 v116, v118, v119
	v_cvt_pk_bf16_f32 v118, v122, v123
	v_pk_add_f32 v[122:123], v[152:153], v[128:129] neg_lo:[0,1] neg_hi:[0,1]
	v_pk_add_f32 v[98:99], v[154:155], v[98:99] neg_lo:[0,1] neg_hi:[0,1]
	v_pk_add_f32 v[100:101], v[156:157], v[100:101] neg_lo:[0,1] neg_hi:[0,1]
	v_pk_add_f32 v[102:103], v[158:159], v[102:103] neg_lo:[0,1] neg_hi:[0,1]
	v_pk_add_f32 v[104:105], v[160:161], v[104:105] neg_lo:[0,1] neg_hi:[0,1]
	v_pk_add_f32 v[106:107], v[202:203], v[106:107] neg_lo:[0,1] neg_hi:[0,1]
	v_pk_add_f32 v[108:109], v[204:205], v[108:109] neg_lo:[0,1] neg_hi:[0,1]
	v_pk_add_f32 v[110:111], v[206:207], v[110:111] neg_lo:[0,1] neg_hi:[0,1]
	v_sub_f32_e32 v113, v209, v113
	v_sub_f32_e32 v112, v208, v112
	v_cvt_pk_bf16_f32 v117, v120, v121
	v_cvt_pk_bf16_f32 v119, v124, v125
	v_cvt_pk_bf16_f32 v120, v126, v127
	v_cvt_pk_bf16_f32 v121, v122, v123
	v_cvt_pk_bf16_f32 v98, v98, v99
	v_cvt_pk_bf16_f32 v99, v100, v101
	v_cvt_pk_bf16_f32 v100, v102, v103
	v_cvt_pk_bf16_f32 v101, v104, v105
	v_cvt_pk_bf16_f32 v102, v106, v107
	v_cvt_pk_bf16_f32 v103, v108, v109
	v_cvt_pk_bf16_f32 v104, v110, v111
	v_cvt_pk_bf16_f32 v105, v112, v113
	ds_read_b128 v[106:109], v190 offset:40960
	ds_read_b128 v[110:113], v190 offset:41984
	ds_read_b128 v[122:125], v190 offset:43008
	ds_read_b128 v[126:129], v190 offset:44032
	ds_read_b128 v[138:141], v190 offset:45056
	ds_read_b128 v[142:145], v190 offset:46080
	ds_read_b128 v[146:149], v190 offset:47104
	ds_read_b128 v[150:153], v190 offset:48128
	s_waitcnt lgkmcnt(8)
	v_mfma_f32_32x32x16_bf16 v[82:97], v[162:165], v[114:117], v[82:97]
	v_mfma_f32_32x32x16_bf16 v[66:81], v[178:181], v[114:117], v[66:81]
	v_mfma_f32_32x32x16_bf16 v[82:97], v[166:169], v[118:121], v[82:97]
	v_mfma_f32_32x32x16_bf16 v[66:81], v[182:185], v[118:121], v[66:81]
	v_mfma_f32_32x32x16_bf16 v[82:97], v[170:173], v[98:101], v[82:97]
	v_mfma_f32_32x32x16_bf16 v[66:81], v[186:189], v[98:101], v[66:81]
	v_mfma_f32_32x32x16_bf16 v[82:97], v[174:177], v[102:105], v[82:97]
	v_mfma_f32_32x32x16_bf16 v[66:81], v[198:201], v[102:105], v[66:81]
	ds_read_b128 v[154:157], v190 offset:49152
	ds_read_b128 v[158:161], v190 offset:50176
	ds_read_b128 v[162:165], v190 offset:51200
	ds_read_b128 v[166:169], v190 offset:52224
	ds_read_b128 v[170:173], v190 offset:53248
	ds_read_b128 v[174:177], v190 offset:54272
	ds_read_b128 v[178:181], v190 offset:55296
	ds_read_b128 v[182:185], v190 offset:56320
	v_pk_mul_f32 v[16:17], v[16:17], v[134:135] op_sel_hi:[1,0]
	v_pk_mul_f32 v[14:15], v[14:15], v[134:135] op_sel_hi:[1,0]
	v_pk_mul_f32 v[12:13], v[12:13], v[134:135] op_sel_hi:[1,0]
	v_pk_mul_f32 v[10:11], v[10:11], v[134:135] op_sel_hi:[1,0]
	v_pk_mul_f32 v[8:9], v[8:9], v[134:135] op_sel_hi:[1,0]
	v_pk_mul_f32 v[6:7], v[6:7], v[134:135] op_sel_hi:[1,0]
	v_pk_mul_f32 v[4:5], v[4:5], v[134:135] op_sel_hi:[1,0]
	v_pk_mul_f32 v[2:3], v[2:3], v[134:135] op_sel_hi:[1,0]
	v_pk_mul_f32 v[32:33], v[32:33], v[134:135] op_sel_hi:[1,0]
	v_pk_mul_f32 v[30:31], v[30:31], v[134:135] op_sel_hi:[1,0]
	v_pk_mul_f32 v[28:29], v[28:29], v[134:135] op_sel_hi:[1,0]
	v_pk_mul_f32 v[26:27], v[26:27], v[134:135] op_sel_hi:[1,0]
	v_pk_mul_f32 v[24:25], v[24:25], v[134:135] op_sel_hi:[1,0]
	v_pk_mul_f32 v[22:23], v[22:23], v[134:135] op_sel_hi:[1,0]
	v_pk_mul_f32 v[20:21], v[20:21], v[134:135] op_sel_hi:[1,0]
	v_pk_mul_f32 v[18:19], v[18:19], v[134:135] op_sel_hi:[1,0]
	s_waitcnt lgkmcnt(8)
	v_mfma_f32_32x32x16_bf16 v[2:17], v[106:109], v[114:117], v[2:17]
	v_mfma_f32_32x32x16_bf16 v[18:33], v[138:141], v[114:117], v[18:33]
	v_mfma_f32_32x32x16_bf16 v[2:17], v[110:113], v[118:121], v[2:17]
	v_mfma_f32_32x32x16_bf16 v[18:33], v[142:145], v[118:121], v[18:33]
	v_mfma_f32_32x32x16_bf16 v[2:17], v[122:125], v[98:101], v[2:17]
	v_mfma_f32_32x32x16_bf16 v[18:33], v[146:149], v[98:101], v[18:33]
	v_mfma_f32_32x32x16_bf16 v[2:17], v[126:129], v[102:105], v[2:17]
	v_mfma_f32_32x32x16_bf16 v[18:33], v[150:153], v[102:105], v[18:33]
	v_mul_f32_e64 v48, v48, v134
	v_mul_f32_e64 v49, v49, v134
	v_mul_f32_e64 v46, v46, v134
	v_mul_f32_e64 v47, v47, v134
	v_mul_f32_e64 v44, v44, v134
	v_mul_f32_e64 v45, v45, v134
	v_pk_mul_f32 v[42:43], v[42:43], v[134:135] op_sel_hi:[1,0]
	v_pk_mul_f32 v[40:41], v[40:41], v[134:135] op_sel_hi:[1,0]
	v_pk_mul_f32 v[38:39], v[38:39], v[134:135] op_sel_hi:[1,0]
	v_pk_mul_f32 v[36:37], v[36:37], v[134:135] op_sel_hi:[1,0]
	v_pk_mul_f32 v[34:35], v[34:35], v[134:135] op_sel_hi:[1,0]
	v_pk_mul_f32 v[64:65], v[64:65], v[134:135] op_sel_hi:[1,0]
	v_pk_mul_f32 v[62:63], v[62:63], v[134:135] op_sel_hi:[1,0]
	v_pk_mul_f32 v[60:61], v[60:61], v[134:135] op_sel_hi:[1,0]
	v_pk_mul_f32 v[58:59], v[58:59], v[134:135] op_sel_hi:[1,0]
	v_pk_mul_f32 v[56:57], v[56:57], v[134:135] op_sel_hi:[1,0]
	v_pk_mul_f32 v[54:55], v[54:55], v[134:135] op_sel_hi:[1,0]
	v_pk_mul_f32 v[52:53], v[52:53], v[134:135] op_sel_hi:[1,0]
	v_pk_mul_f32 v[50:51], v[50:51], v[134:135] op_sel_hi:[1,0]
	s_waitcnt lgkmcnt(0)
	v_mfma_f32_32x32x16_bf16 v[34:49], v[154:157], v[114:117], v[34:49]
	s_mov_b64 s[8:9], -1
	s_cmpk_gt_i32 s10, 0xff
	v_mfma_f32_32x32x16_bf16 v[50:65], v[170:173], v[114:117], v[50:65]
	v_mfma_f32_32x32x16_bf16 v[34:49], v[158:161], v[118:121], v[34:49]
	v_mfma_f32_32x32x16_bf16 v[50:65], v[174:177], v[118:121], v[50:65]
	v_mfma_f32_32x32x16_bf16 v[34:49], v[162:165], v[98:101], v[34:49]
	v_mfma_f32_32x32x16_bf16 v[50:65], v[178:181], v[98:101], v[50:65]
	v_mfma_f32_32x32x16_bf16 v[34:49], v[166:169], v[102:105], v[34:49]
	v_mfma_f32_32x32x16_bf16 v[50:65], v[182:185], v[102:105], v[50:65]
	s_cbranch_scc0 .LBB0_771
	s_lshl_b32 s11, s10, 6
	s_mov_b64 s[8:9], 0
